# attention half-step top: K LDS-DMA pieces issued before the V wait / LDS write (counted vmcnt); B-half DMA address temporaries renamed to v106..v111
# baseline (speedup 1.0000x reference)
; #define VWRITE(b) do { *(LAS bf16x8*)(V_lds + (b) * SHM_V + vst0) = vs0; *(LAS bf16x8*)(V_lds + (b) * SHM_V + vst1) = vs1; } while (0)
; #define SWAIT() asm volatile("s_waitcnt vmcnt(0)" ::: "memory")
; __device__ __forceinline__ void attn_unit(const bf16* __restrict__ Qraw, const float* __restrict__ ssq, const float* __restrict__ qn, int t0, const bf16* __restrict__ Kh, const bf16* __restrict__ Vh, bf16* __restrict__ Ob, int seq, LAS char* lds, int tid) {
;     ...
;     for (int h = 1; h + 1 < NT; h += 2) {
;         SWAIT(); VWRITE(1); DMA_K((h + 1) * KVBLK, 0);
.LBB0_1462:
	s_add_u32 s10, s2, s60
	v_mov_b32_e32 v146, v192
	v_mov_b32_e32 v66, v194
	v_mov_b32_e32 v68, v193
	s_addc_u32 s11, s3, s59
	v_mov_b32_e32 v69, v147
	v_lshl_add_u64 v[70:71], s[10:11], 0, v[146:147]
	s_mov_b32 m0, s62
	v_lshl_add_u64 v[70:71], v[70:71], 0, s[0:1]
	v_lshl_add_u64 v[68:69], s[10:11], 0, v[68:69]
	v_mov_b32_e32 v67, v147
	global_load_lds_dwordx4 v[70:71], off
	v_lshl_add_u64 v[68:69], v[68:69], 0, s[0:1]
	s_mov_b32 m0, s63
	v_lshl_add_u64 v[66:67], s[10:11], 0, v[66:67]
	global_load_lds_dwordx4 v[68:69], off
	v_lshl_add_u64 v[66:67], v[66:67], 0, s[0:1]
	s_mov_b32 m0, s64
	s_and_b64 vcc, exec, s[42:43]
	global_load_lds_dwordx4 v[66:67], off
	s_waitcnt vmcnt(4)
	ds_write_b128 v198, v[114:117] offset:16384
	s_waitcnt vmcnt(3)
	ds_write_b128 v199, v[118:121] offset:16384
	s_cbranch_vccnz .LBB0_1464
	s_add_u32 s10, s2, s60
	v_mov_b32_e32 v146, v196
	s_addc_u32 s11, s3, s59
	s_add_i32 m0, s61, 0xe000
	v_lshl_add_u64 v[66:67], s[10:11], 0, v[146:147]
	v_lshl_add_u64 v[66:67], v[66:67], 0, s[0:1]
	global_load_lds_dwordx4 v[66:67], off

; #define VWRITE(b) do { *(LAS bf16x8*)(V_lds + (b) * SHM_V + vst0) = vs0; *(LAS bf16x8*)(V_lds + (b) * SHM_V + vst1) = vs1; } while (0)
; #define KWAIT_BAR(nv) do { if ((nv) == 2) asm volatile("s_waitcnt vmcnt(2)" ::: "memory"); else asm volatile("s_waitcnt vmcnt(0)" ::: "memory"); __syncthreads(); } while (0)
; #define SWAIT() asm volatile("s_waitcnt vmcnt(0)" ::: "memory")
; __device__ __forceinline__ void attn_unit(const bf16* __restrict__ Qraw, const float* __restrict__ ssq, const float* __restrict__ qn, int t0, const bf16* __restrict__ Kh, const bf16* __restrict__ Vh, bf16* __restrict__ Ob, int seq, LAS char* lds, int tid) {
;     ...
;         KWAIT_BAR(2);
;         SWAIT(); VWRITE(0); DMA_K((h + 2) * KVBLK, 1);
.LBB0_1466:
	s_add_u32 s10, s2, s60
	s_waitcnt vmcnt(2)
	s_barrier
	v_mov_b32_e32 v146, v192
	v_mov_b32_e32 v106, v194
	v_mov_b32_e32 v108, v193
	s_addc_u32 s11, s3, s59
	v_mov_b32_e32 v109, v147
	v_lshl_add_u64 v[110:111], s[10:11], 0, v[146:147]
	s_mov_b32 m0, s36
	v_lshl_add_u64 v[110:111], v[110:111], 0, s[28:29]
	v_lshl_add_u64 v[108:109], s[10:11], 0, v[108:109]
	v_mov_b32_e32 v107, v147
	global_load_lds_dwordx4 v[110:111], off
	v_lshl_add_u64 v[108:109], v[108:109], 0, s[28:29]
	s_add_i32 m0, s36, 0x2000
	v_lshl_add_u64 v[106:107], s[10:11], 0, v[106:107]
	global_load_lds_dwordx4 v[108:109], off
	v_lshl_add_u64 v[106:107], v[106:107], 0, s[28:29]
	s_add_i32 m0, s36, 0x4000
	s_and_b64 vcc, exec, s[42:43]
	global_load_lds_dwordx4 v[106:107], off
	s_waitcnt vmcnt(4)
	ds_write_b128 v198, v[98:101]
	s_waitcnt vmcnt(3)
	ds_write_b128 v199, v[102:105]
	s_cbranch_vccnz .LBB0_1468
	s_add_u32 s10, s2, s60
	v_mov_b32_e32 v146, v196
	s_addc_u32 s11, s3, s59
	s_add_i32 m0, s36, 0x6000
	v_lshl_add_u64 v[106:107], s[10:11], 0, v[146:147]
	v_lshl_add_u64 v[106:107], v[106:107], 0, s[28:29]
	global_load_lds_dwordx4 v[106:107], off
